# code placement scan: v045 + code between the two attention regions shifted +8 bytes
# speedup vs baseline: 1.0037x; 1.0037x over previous
.LBB0_342:
	s_cmp_lg_u32 0, -1
	s_cselect_b32 s0, 0, 0
	s_addk_i32 s0, 0x6000
	v_add3_u32 v8, v237, s0, v233
	s_add_i32 s0, s33, 0x4000
	v_add_f32_e32 v2, v243, v2
	s_and_b32 s0, s0, 0xffff
	v_add3_u32 v16, v8, v236, s0
	ds_read_b64_tr_b16 v[8:9],v16 offset:0
	ds_read_b64_tr_b16 v[10:11],v16 offset:512
	ds_read_b64_tr_b16 v[12:13],v16 offset:1024
	ds_read_b64_tr_b16 v[14:15],v16 offset:1536
	ds_read_b64_tr_b16 v[82:83],v16 offset:2048
	ds_read_b64_tr_b16 v[84:85],v16 offset:2560
	ds_read_b64_tr_b16 v[86:87],v16 offset:3072
	ds_read_b64_tr_b16 v[88:89],v16 offset:3584
	s_waitcnt lgkmcnt(0)
	s_nop 0
	v_mfma_f32_32x32x16_bf16 v[66:81], v[138:141], v[8:11], v[66:81]
	ds_read_b64_tr_b16 v[8:9],v16 offset:4096
	ds_read_b64_tr_b16 v[10:11],v16 offset:4608
	v_mfma_f32_32x32x16_bf16 v[66:81], v[134:137], v[12:15], v[66:81]
	ds_read_b64_tr_b16 v[12:13],v16 offset:5120
	ds_read_b64_tr_b16 v[14:15],v16 offset:5632
	v_mfma_f32_32x32x16_bf16 v[66:81], v[130:133], v[82:85], v[66:81]
	ds_read_b64_tr_b16 v[82:83],v16 offset:6144
	ds_read_b64_tr_b16 v[84:85],v16 offset:6656
	ds_read_b64_tr_b16 v[90:91],v16 offset:7168
	ds_read_b64_tr_b16 v[92:93],v16 offset:7680
	s_waitcnt lgkmcnt(0)
	v_mfma_f32_32x32x16_bf16 v[66:81], v[4:7], v[86:89], v[66:81]
	v_mfma_f32_32x32x16_bf16 v[50:65], v[138:141], v[8:11], v[50:65]
	v_add_u32_e32 v16, 0x2000, v16
	ds_read_b64_tr_b16 v[8:9],v16 offset:0
	ds_read_b64_tr_b16 v[10:11],v16 offset:512
	v_mfma_f32_32x32x16_bf16 v[50:65], v[134:137], v[12:15], v[50:65]
	ds_read_b64_tr_b16 v[12:13],v16 offset:1024
	ds_read_b64_tr_b16 v[14:15],v16 offset:1536
	v_mfma_f32_32x32x16_bf16 v[50:65], v[130:133], v[82:85], v[50:65]
	ds_read_b64_tr_b16 v[82:83],v16 offset:2048
	ds_read_b64_tr_b16 v[84:85],v16 offset:2560
	ds_read_b64_tr_b16 v[86:87],v16 offset:3072
	ds_read_b64_tr_b16 v[88:89],v16 offset:3584
	s_waitcnt lgkmcnt(0)
	v_mfma_f32_32x32x16_bf16 v[50:65], v[4:7], v[90:93], v[50:65]
	v_mfma_f32_32x32x16_bf16 v[34:49], v[138:141], v[8:11], v[34:49]
	ds_read_b64_tr_b16 v[8:9],v16 offset:4096
	ds_read_b64_tr_b16 v[10:11],v16 offset:4608
	v_mfma_f32_32x32x16_bf16 v[34:49], v[134:137], v[12:15], v[34:49]
	ds_read_b64_tr_b16 v[12:13],v16 offset:5120
	ds_read_b64_tr_b16 v[14:15],v16 offset:5632
	v_mfma_f32_32x32x16_bf16 v[34:49], v[130:133], v[82:85], v[34:49]
	ds_read_b64_tr_b16 v[82:83],v16 offset:6144
	ds_read_b64_tr_b16 v[84:85],v16 offset:6656
	ds_read_b64_tr_b16 v[90:91],v16 offset:7168
	ds_read_b64_tr_b16 v[92:93],v16 offset:7680
	s_waitcnt lgkmcnt(0)
	v_mfma_f32_32x32x16_bf16 v[34:49], v[4:7], v[86:89], v[34:49]
	v_mfma_f32_32x32x16_bf16 v[18:33], v[138:141], v[8:11], v[18:33]
	v_mov_b32_e32 v8, v2
	s_nop 1
	v_permlane32_swap_b32_e32 v2, v8
	v_cmp_gt_u32_e32 vcc, 32, v230
	v_mfma_f32_32x32x16_bf16 v[18:33], v[134:137], v[12:15], v[18:33]
	v_mfma_f32_32x32x16_bf16 v[18:33], v[130:133], v[82:85], v[18:33]
	v_mfma_f32_32x32x16_bf16 v[18:33], v[4:7], v[90:93], v[18:33]
	s_and_saveexec_b64 s[0:1], vcc
	v_add_f32_e32 v2, v2, v8
	ds_write_b32 v235, v2 offset:128
	s_or_b64 exec, exec, s[0:1]
	s_waitcnt lgkmcnt(0)
	ds_read_b128 v[4:7], v234 offset:128
	ds_read_b128 v[8:11], v234 offset:160
	s_lshl_b32 s0, s84, 8
	s_add_u32 s2, s6, s0
	s_addc_u32 s3, s7, 0
	s_waitcnt lgkmcnt(1)
	v_rcp_f32_e32 v14, v4
	v_rcp_f32_e32 v15, v5
	v_rcp_f32_e32 v16, v6
	v_rcp_f32_e32 v17, v7
	ds_read_b128 v[4:7], v234 offset:192
	s_lshl_b64 s[0:1], s[34:35], 11
	s_add_u32 s0, s2, s0
	s_addc_u32 s1, s3, s1
	s_lshl_b32 s2, s83, 12
	s_add_i32 s2, s2, 0
	v_lshlrev_b32_e32 v2, 1, v232
	s_add_i32 s2, s2, 0x16800
	v_and_b32_e32 v2, 0x70, v2
	s_waitcnt lgkmcnt(1)
	v_rcp_f32_e32 v82, v8
	v_rcp_f32_e32 v83, v9
	v_rcp_f32_e32 v84, v10
	v_rcp_f32_e32 v85, v11
	ds_read_b128 v[8:11], v234 offset:224
	s_waitcnt lgkmcnt(1)
	v_rcp_f32_e32 v86, v4
	v_lshlrev_b32_e32 v4, 1, v231
	v_add_u32_e32 v95, s2, v2
	v_lshl_add_u64 v[12:13], s[0:1], 0, v[2:3]
	v_lshlrev_b32_e32 v2, 9, v229
	v_add3_u32 v97, s2, v4, v2
	v_mul_f32_e32 v2, v66, v14
	v_cvt_pk_bf16_f32 v2, v2, s0
	ds_write_b16 v97, v2
	v_mul_f32_e32 v2, v50, v14
	v_cvt_pk_bf16_f32 v2, v2, s0
	ds_write_b16 v97, v2 offset:64
	v_mul_f32_e32 v2, v67, v15
	v_cvt_pk_bf16_f32 v2, v2, s0
	ds_write_b16 v97, v2 offset:128
	v_mul_f32_e32 v2, v51, v15
	v_cvt_pk_bf16_f32 v2, v2, s0
	ds_write_b16 v97, v2 offset:192
	v_mul_f32_e32 v2, v68, v16
	v_cvt_pk_bf16_f32 v2, v2, s0
	ds_write_b16 v97, v2 offset:256
	v_mul_f32_e32 v2, v52, v16
	v_cvt_pk_bf16_f32 v2, v2, s0
	ds_write_b16 v97, v2 offset:320
	v_mul_f32_e32 v2, v69, v17
	v_cvt_pk_bf16_f32 v2, v2, s0
	ds_write_b16 v97, v2 offset:384
	v_mul_f32_e32 v2, v53, v17
	v_cvt_pk_bf16_f32 v2, v2, s0
	ds_write_b16 v97, v2 offset:448
	v_mul_f32_e32 v2, v70, v82
	v_cvt_pk_bf16_f32 v2, v2, s0
	ds_write_b16 v97, v2 offset:1024
	v_mul_f32_e32 v2, v54, v82
	v_cvt_pk_bf16_f32 v2, v2, s0
	ds_write_b16 v97, v2 offset:1088
	v_mul_f32_e32 v2, v71, v83
	v_cvt_pk_bf16_f32 v2, v2, s0
	ds_write_b16 v97, v2 offset:1152
	v_mul_f32_e32 v2, v55, v83
	v_cvt_pk_bf16_f32 v2, v2, s0
	ds_write_b16 v97, v2 offset:1216
	v_mul_f32_e32 v2, v72, v84
	v_cvt_pk_bf16_f32 v2, v2, s0
	ds_write_b16 v97, v2 offset:1280
	v_mul_f32_e32 v2, v56, v84
	v_cvt_pk_bf16_f32 v2, v2, s0
	ds_write_b16 v97, v2 offset:1344
	v_mul_f32_e32 v2, v73, v85
	v_cvt_pk_bf16_f32 v2, v2, s0
	ds_write_b16 v97, v2 offset:1408
	v_mul_f32_e32 v2, v57, v85
	v_cvt_pk_bf16_f32 v2, v2, s0
	v_rcp_f32_e32 v87, v5
	ds_write_b16 v97, v2 offset:1472
	v_mul_f32_e32 v2, v74, v86
	v_cvt_pk_bf16_f32 v2, v2, s0
	ds_write_b16 v97, v2 offset:2048
	v_mul_f32_e32 v2, v58, v86
	v_cvt_pk_bf16_f32 v2, v2, s0
	v_rcp_f32_e32 v88, v6
	ds_write_b16 v97, v2 offset:2112
	v_mul_f32_e32 v2, v75, v87
	v_cvt_pk_bf16_f32 v2, v2, s0
	ds_write_b16 v97, v2 offset:2176
	v_mul_f32_e32 v2, v59, v87
	v_cvt_pk_bf16_f32 v2, v2, s0
	v_rcp_f32_e32 v89, v7
	ds_write_b16 v97, v2 offset:2240
	v_mul_f32_e32 v2, v76, v88
	v_cvt_pk_bf16_f32 v2, v2, s0
	ds_write_b16 v97, v2 offset:2304
	v_mul_f32_e32 v2, v60, v88
	v_cvt_pk_bf16_f32 v2, v2, s0
	s_waitcnt lgkmcnt(14)
	v_rcp_f32_e32 v90, v8
	ds_write_b16 v97, v2 offset:2368
	v_mul_f32_e32 v2, v77, v89
	v_cvt_pk_bf16_f32 v2, v2, s0
	ds_write_b16 v97, v2 offset:2432
	v_mul_f32_e32 v2, v61, v89
	v_cvt_pk_bf16_f32 v2, v2, s0
	v_rcp_f32_e32 v91, v9
	ds_write_b16 v97, v2 offset:2496
	v_mul_f32_e32 v2, v78, v90
	v_cvt_pk_bf16_f32 v2, v2, s0
	ds_write_b16 v97, v2 offset:3072
	v_mul_f32_e32 v2, v62, v90
	v_cvt_pk_bf16_f32 v2, v2, s0
	v_rcp_f32_e32 v92, v10
	ds_write_b16 v97, v2 offset:3136
	v_mul_f32_e32 v2, v79, v91
	v_cvt_pk_bf16_f32 v2, v2, s0
	ds_write_b16 v97, v2 offset:3200
	v_mul_f32_e32 v2, v63, v91
	v_cvt_pk_bf16_f32 v2, v2, s0
	v_rcp_f32_e32 v93, v11
	ds_write_b16 v97, v2 offset:3264
	v_mul_f32_e32 v2, v80, v92
	v_cvt_pk_bf16_f32 v2, v2, s0
	ds_write_b16 v97, v2 offset:3328
	v_mul_f32_e32 v2, v64, v92
	v_cvt_pk_bf16_f32 v2, v2, s0
	ds_write_b16 v97, v2 offset:3392
	v_mul_f32_e32 v2, v81, v93
	v_cvt_pk_bf16_f32 v2, v2, s0
	ds_write_b16 v97, v2 offset:3456
	v_mul_f32_e32 v2, v65, v93
	v_lshrrev_b32_e32 v94, 3, v230
	v_cvt_pk_bf16_f32 v2, v2, s0
	ds_write_b16 v97, v2 offset:3520
	v_or_b32_e32 v52, 8, v94
	v_lshl_add_u32 v96, v94, 7, v95
	s_waitcnt lgkmcnt(0)
	v_lshl_add_u32 v58, v52, 7, v95
	ds_read_b128 v[4:7], v96
	ds_read_b128 v[8:11], v58
	v_lshlrev_b32_e32 v2, 11, v94
	v_lshl_add_u64 v[50:51], v[12:13], 0, v[2:3]
	v_lshlrev_b32_e32 v2, 11, v52
	v_lshl_add_u64 v[52:53], v[12:13], 0, v[2:3]
	v_or_b32_e32 v2, 16, v94
	v_or_b32_e32 v56, 24, v94
	v_lshl_add_u32 v59, v2, 7, v95
	v_lshl_add_u32 v60, v56, 7, v95
	s_waitcnt lgkmcnt(1)
	global_store_dwordx4 v[50:51], v[4:7], off
	ds_read_b128 v[4:7], v59
	s_waitcnt lgkmcnt(1)
	global_store_dwordx4 v[52:53], v[8:11], off
	ds_read_b128 v[8:11], v60
	v_lshlrev_b32_e32 v2, 11, v2
	v_lshl_add_u64 v[54:55], v[12:13], 0, v[2:3]
	v_lshlrev_b32_e32 v2, 11, v56
	v_lshl_add_u64 v[56:57], v[12:13], 0, v[2:3]
	v_mul_f32_e32 v2, v34, v14
	s_waitcnt lgkmcnt(1)
	global_store_dwordx4 v[54:55], v[4:7], off
	s_waitcnt lgkmcnt(0)
	global_store_dwordx4 v[56:57], v[8:11], off
	v_cvt_pk_bf16_f32 v2, v2, s0
	s_waitcnt lgkmcnt(0)
	ds_write_b16 v97, v2
	v_mul_f32_e32 v2, v18, v14
	v_cvt_pk_bf16_f32 v2, v2, s0
	ds_write_b16 v97, v2 offset:64
	v_mul_f32_e32 v2, v35, v15
	v_cvt_pk_bf16_f32 v2, v2, s0
	ds_write_b16 v97, v2 offset:128
	v_mul_f32_e32 v2, v19, v15
	v_cvt_pk_bf16_f32 v2, v2, s0
	ds_write_b16 v97, v2 offset:192
	v_mul_f32_e32 v2, v36, v16
	v_cvt_pk_bf16_f32 v2, v2, s0
	ds_write_b16 v97, v2 offset:256
	v_mul_f32_e32 v2, v20, v16
	v_cvt_pk_bf16_f32 v2, v2, s0
	ds_write_b16 v97, v2 offset:320
	v_mul_f32_e32 v2, v37, v17
	v_cvt_pk_bf16_f32 v2, v2, s0
	ds_write_b16 v97, v2 offset:384
	v_mul_f32_e32 v2, v21, v17
	v_cvt_pk_bf16_f32 v2, v2, s0
	ds_write_b16 v97, v2 offset:448
	v_mul_f32_e32 v2, v38, v82
	v_cvt_pk_bf16_f32 v2, v2, s0
	ds_write_b16 v97, v2 offset:1024
	v_mul_f32_e32 v2, v22, v82
	v_cvt_pk_bf16_f32 v2, v2, s0
	ds_write_b16 v97, v2 offset:1088
	v_mul_f32_e32 v2, v39, v83
	v_cvt_pk_bf16_f32 v2, v2, s0
	ds_write_b16 v97, v2 offset:1152
	v_mul_f32_e32 v2, v23, v83
	v_cvt_pk_bf16_f32 v2, v2, s0
	ds_write_b16 v97, v2 offset:1216
	v_mul_f32_e32 v2, v40, v84
	v_cvt_pk_bf16_f32 v2, v2, s0
	ds_write_b16 v97, v2 offset:1280
	v_mul_f32_e32 v2, v24, v84
	v_cvt_pk_bf16_f32 v2, v2, s0
	ds_write_b16 v97, v2 offset:1344
	v_mul_f32_e32 v2, v41, v85
	v_cvt_pk_bf16_f32 v2, v2, s0
	ds_write_b16 v97, v2 offset:1408
	v_mul_f32_e32 v2, v25, v85
	v_cvt_pk_bf16_f32 v2, v2, s0
	ds_write_b16 v97, v2 offset:1472
	v_mul_f32_e32 v2, v42, v86
	v_cvt_pk_bf16_f32 v2, v2, s0
	ds_write_b16 v97, v2 offset:2048
	v_mul_f32_e32 v2, v26, v86
	v_cvt_pk_bf16_f32 v2, v2, s0
	ds_write_b16 v97, v2 offset:2112
	v_mul_f32_e32 v2, v43, v87
	v_cvt_pk_bf16_f32 v2, v2, s0
	ds_write_b16 v97, v2 offset:2176
	v_mul_f32_e32 v2, v27, v87
	v_cvt_pk_bf16_f32 v2, v2, s0
	ds_write_b16 v97, v2 offset:2240
	v_mul_f32_e32 v2, v44, v88
	v_cvt_pk_bf16_f32 v2, v2, s0
	ds_write_b16 v97, v2 offset:2304
	v_mul_f32_e32 v2, v28, v88
	v_cvt_pk_bf16_f32 v2, v2, s0
	ds_write_b16 v97, v2 offset:2368
	v_mul_f32_e32 v2, v45, v89
	v_cvt_pk_bf16_f32 v2, v2, s0
	ds_write_b16 v97, v2 offset:2432
	v_mul_f32_e32 v2, v29, v89
	v_cvt_pk_bf16_f32 v2, v2, s0
	ds_write_b16 v97, v2 offset:2496
	v_mul_f32_e32 v2, v46, v90
	v_cvt_pk_bf16_f32 v2, v2, s0
	ds_write_b16 v97, v2 offset:3072
	v_mul_f32_e32 v2, v30, v90
	v_cvt_pk_bf16_f32 v2, v2, s0
	ds_write_b16 v97, v2 offset:3136
	v_mul_f32_e32 v2, v47, v91
	v_cvt_pk_bf16_f32 v2, v2, s0
	ds_write_b16 v97, v2 offset:3200
	v_mul_f32_e32 v2, v31, v91
	v_cvt_pk_bf16_f32 v2, v2, s0
	ds_write_b16 v97, v2 offset:3264
	v_mul_f32_e32 v2, v48, v92
	v_cvt_pk_bf16_f32 v2, v2, s0
	ds_write_b16 v97, v2 offset:3328
	v_mul_f32_e32 v2, v32, v92
	v_cvt_pk_bf16_f32 v2, v2, s0
	ds_write_b16 v97, v2 offset:3392
	v_mul_f32_e32 v2, v49, v93
	v_cvt_pk_bf16_f32 v2, v2, s0
	ds_write_b16 v97, v2 offset:3456
	v_mul_f32_e32 v2, v33, v93
	v_cvt_pk_bf16_f32 v2, v2, s0
	ds_write_b16 v97, v2 offset:3520
	s_waitcnt lgkmcnt(0)
	ds_read_b128 v[4:7], v96
	ds_read_b128 v[8:11], v58
	ds_read_b128 v[12:15], v59
	ds_read_b128 v[16:19], v60
	s_waitcnt lgkmcnt(3)
	global_store_dwordx4 v[50:51], v[4:7], off offset:128
	s_waitcnt lgkmcnt(2)
	global_store_dwordx4 v[52:53], v[8:11], off offset:128
	s_waitcnt lgkmcnt(1)
	global_store_dwordx4 v[54:55], v[12:15], off offset:128
	s_waitcnt lgkmcnt(0)
	global_store_dwordx4 v[56:57], v[16:19], off offset:128
	s_waitcnt lgkmcnt(0)
	s_waitcnt lgkmcnt(0)
	s_barrier
	s_cmp_lt_u32 s21, 2
	s_cbranch_scc1 .LBB0_259
	v_mov_b32_e32 v6, v0
	s_lshl_b32 s0, s82, 8
	v_ashrrev_i32_e32 v4, 1, v6
	s_or_b32 s0, s8, s0
	s_mov_b32 s1, s9
	v_ashrrev_i32_e32 v5, 31, v4
	v_lshl_add_u64 v[12:13], s[0:1], 0, v[4:5]
	v_lshlrev_b32_e32 v2, 6, v6
	v_lshlrev_b64 v[4:5], 11, v[12:13]
	v_and_b32_e32 v7, 64, v2
	v_lshl_add_u64 v[4:5], s[6:7], 0, v[4:5]
	v_lshlrev_b32_e32 v2, 1, v7
	v_lshl_add_u64 v[4:5], v[4:5], 0, v[2:3]
	s_waitcnt vmcnt(0)
	s_barrier
	global_load_dwordx2 v[16:17], v[4:5], off sc1
	global_load_dwordx2 v[18:19], v[4:5], off offset:256 sc1
	global_load_dwordx2 v[24:25], v[4:5], off offset:8 sc1
	global_load_dwordx2 v[26:27], v[4:5], off offset:264 sc1
	global_load_dwordx2 v[30:31], v[4:5], off offset:16 sc1
	global_load_dwordx2 v[34:35], v[4:5], off offset:272 sc1
	global_load_dwordx2 v[42:43], v[4:5], off offset:24 sc1
	global_load_dwordx2 v[50:51], v[4:5], off offset:280 sc1
	v_lshlrev_b32_e32 v6, 2, v6
	v_bitop3_b32 v83, v6, 4, v228 bitop3:0x6c
	v_lshlrev_b32_e32 v82, 2, v7
	global_load_dwordx2 v[54:55], v[4:5], off offset:32 sc1
	global_load_dwordx2 v[60:61], v[4:5], off offset:288 sc1
	global_load_dwordx2 v[74:75], v[4:5], off offset:40 sc1
	global_load_dwordx2 v[84:85], v[4:5], off offset:296 sc1
	global_load_dwordx2 v[86:87], v[4:5], off offset:48 sc1
	global_load_dwordx2 v[88:89], v[4:5], off offset:304 sc1
	global_load_dwordx2 v[90:91], v[4:5], off offset:56 sc1
	global_load_dwordx2 v[28:29], v[4:5], off offset:312 sc1
	global_load_dwordx2 v[58:59], v[4:5], off offset:64 sc1
	global_load_dwordx2 v[36:37], v[4:5], off offset:320 sc1
	global_load_dwordx2 v[66:67], v[4:5], off offset:72 sc1
	global_load_dwordx2 v[44:45], v[4:5], off offset:328 sc1
	global_load_dwordx2 v[62:63], v[4:5], off offset:80 sc1
	global_load_dwordx2 v[52:53], v[4:5], off offset:336 sc1
	global_load_dwordx2 v[76:77], v[4:5], off offset:88 sc1
	global_load_dwordx2 v[32:33], v[4:5], off offset:344 sc1
	global_load_dwordx2 v[68:69], v[4:5], off offset:96 sc1
	global_load_dwordx2 v[38:39], v[4:5], off offset:352 sc1
	global_load_dwordx2 v[80:81], v[4:5], off offset:104 sc1
	global_load_dwordx2 v[20:21], v[4:5], off offset:360 sc1
	global_load_dwordx2 v[46:47], v[4:5], off offset:112 sc1
	global_load_dwordx2 v[22:23], v[4:5], off offset:368 sc1
	global_load_dwordx2 v[56:57], v[4:5], off offset:120 sc1
	global_load_dwordx2 v[48:49], v[4:5], off offset:376 sc1
	s_nop 0
	global_load_dwordx4 v[4:7], v82, s[58:59] offset:16
	global_load_dwordx4 v[8:11], v82, s[58:59]
	v_mov_b64_e32 v[14:15], s[24:25]
	v_mad_u64_u32 v[14:15], s[0:1], v12, s5, v[14:15]
	v_mad_i32_i24 v15, v13, s5, v15
	v_lshl_add_u64 v[12:13], v[14:15], 0, v[2:3]
	s_mov_b32 s0, 0xf800000
	s_waitcnt vmcnt(33)
	v_lshlrev_b32_e32 v41, 16, v17
	v_lshlrev_b32_e32 v40, 16, v16
	s_waitcnt vmcnt(32)
	v_lshlrev_b32_e32 v65, 16, v19
	v_lshlrev_b32_e32 v64, 16, v18
	v_and_b32_e32 v17, 0xffff0000, v17
	v_and_b32_e32 v16, 0xffff0000, v16
	v_and_b32_e32 v19, 0xffff0000, v19
	v_and_b32_e32 v18, 0xffff0000, v18
	s_waitcnt vmcnt(29)
	v_lshlrev_b32_e32 v95, 16, v31
	v_lshlrev_b32_e32 v94, 16, v30
	s_waitcnt vmcnt(28)
	v_lshlrev_b32_e32 v97, 16, v35
	v_lshlrev_b32_e32 v96, 16, v34
	v_and_b32_e32 v31, 0xffff0000, v31
	v_and_b32_e32 v30, 0xffff0000, v30
	v_and_b32_e32 v35, 0xffff0000, v35
	v_and_b32_e32 v34, 0xffff0000, v34
	v_pk_fma_f32 v[72:73], v[214:215], v[18:19], v[16:17] neg_lo:[1,0,0] neg_hi:[1,0,0]
	v_pk_fma_f32 v[18:19], v[214:215], v[96:97], v[94:95] neg_lo:[1,0,0] neg_hi:[1,0,0]
	v_pk_fma_f32 v[16:17], v[214:215], v[34:35], v[30:31] neg_lo:[1,0,0] neg_hi:[1,0,0]
	v_lshlrev_b32_e32 v71, 16, v25
	v_lshlrev_b32_e32 v70, 16, v24
	v_lshlrev_b32_e32 v93, 16, v27
	v_lshlrev_b32_e32 v92, 16, v26
	v_and_b32_e32 v25, 0xffff0000, v25
	v_and_b32_e32 v24, 0xffff0000, v24
	v_and_b32_e32 v27, 0xffff0000, v27
	v_and_b32_e32 v26, 0xffff0000, v26
	v_mov_b32_e32 v30, v18
	v_mov_b32_e32 v31, v16
	v_mul_f32_e32 v34, v16, v16
	v_pk_fma_f32 v[78:79], v[214:215], v[64:65], v[40:41] neg_lo:[1,0,0] neg_hi:[1,0,0]
	v_pk_fma_f32 v[64:65], v[214:215], v[26:27], v[24:25] neg_lo:[1,0,0] neg_hi:[1,0,0]
	v_pk_fma_f32 v[30:31], v[30:31], v[30:31], v[34:35] op_sel_hi:[1,1,0]
	v_mov_b32_e32 v34, v19
	v_mov_b32_e32 v35, v17
	v_mul_f32_e32 v40, v17, v17
	v_pk_fma_f32 v[70:71], v[214:215], v[92:93], v[70:71] neg_lo:[1,0,0] neg_hi:[1,0,0]
	v_pk_mul_f32 v[24:25], v[72:73], v[72:73]
	v_pk_mul_f32 v[26:27], v[64:65], v[64:65]
	v_pk_fma_f32 v[34:35], v[34:35], v[34:35], v[40:41] op_sel_hi:[1,1,0]
	s_waitcnt vmcnt(27)
	v_lshlrev_b32_e32 v41, 16, v43
	v_lshlrev_b32_e32 v40, 16, v42
	s_waitcnt vmcnt(26)
	v_lshlrev_b32_e32 v93, 16, v51
	v_lshlrev_b32_e32 v92, 16, v50
	v_and_b32_e32 v43, 0xffff0000, v43
	v_and_b32_e32 v42, 0xffff0000, v42
	v_and_b32_e32 v51, 0xffff0000, v51
	v_and_b32_e32 v50, 0xffff0000, v50
	v_pk_fma_f32 v[24:25], v[78:79], v[78:79], v[24:25]
	v_pk_fma_f32 v[26:27], v[70:71], v[70:71], v[26:27]
	v_pk_fma_f32 v[40:41], v[214:215], v[92:93], v[40:41] neg_lo:[1,0,0] neg_hi:[1,0,0]
	v_pk_fma_f32 v[50:51], v[214:215], v[50:51], v[42:43] neg_lo:[1,0,0] neg_hi:[1,0,0]
	v_pk_add_f32 v[24:25], v[24:25], v[24:25] op_sel:[0,1] op_sel_hi:[1,0]
	v_pk_add_f32 v[26:27], v[26:27], v[26:27] op_sel:[0,1] op_sel_hi:[1,0]
	v_pk_mul_f32 v[42:43], v[40:41], v[40:41]
	v_pk_mul_f32 v[92:93], v[50:51], v[50:51]
	v_mov_b32_e32 v25, v42
	v_mov_b32_e32 v27, v92
	v_mov_b32_e32 v31, v43
	v_mov_b32_e32 v35, v93
	v_pk_add_f32 v[24:25], v[24:25], v[26:27]
	v_pk_add_f32 v[26:27], v[30:31], v[34:35]
	s_waitcnt vmcnt(24)
	v_and_b32_e32 v31, 0xffff0000, v61
	v_pk_add_f32 v[24:25], v[24:25], v[26:27]
	v_lshlrev_b32_e32 v27, 16, v61
	v_pk_add_f32 v[92:93], v[24:25], v[24:25] op_sel:[0,1] op_sel_hi:[1,0]
	v_lshlrev_b32_e32 v25, 16, v55
	v_lshlrev_b32_e32 v24, 16, v54
	v_lshlrev_b32_e32 v26, 16, v60
	v_pk_fma_f32 v[26:27], v[214:215], v[26:27], v[24:25] neg_lo:[1,0,0] neg_hi:[1,0,0]
	v_and_b32_e32 v25, 0xffff0000, v55
	v_and_b32_e32 v24, 0xffff0000, v54
	v_and_b32_e32 v30, 0xffff0000, v60
	v_pk_fma_f32 v[34:35], v[214:215], v[30:31], v[24:25] neg_lo:[1,0,0] neg_hi:[1,0,0]
	s_waitcnt vmcnt(22)
	v_lshlrev_b32_e32 v31, 16, v85
	v_pk_mul_f32 v[24:25], v[34:35], v[34:35]
	v_lshlrev_b32_e32 v30, 16, v84
	v_pk_fma_f32 v[24:25], v[26:27], v[26:27], v[24:25]
	s_waitcnt vmcnt(0)
	v_mov_b32_e32 v15, v10
	v_pk_add_f32 v[60:61], v[24:25], v[24:25] op_sel:[0,1] op_sel_hi:[1,0]
	v_lshlrev_b32_e32 v25, 16, v75
	v_lshlrev_b32_e32 v24, 16, v74
	v_pk_fma_f32 v[42:43], v[214:215], v[30:31], v[24:25] neg_lo:[1,0,0] neg_hi:[1,0,0]
	v_and_b32_e32 v25, 0xffff0000, v75
	v_and_b32_e32 v24, 0xffff0000, v74
	v_and_b32_e32 v31, 0xffff0000, v85
	v_and_b32_e32 v30, 0xffff0000, v84
	v_pk_fma_f32 v[54:55], v[214:215], v[30:31], v[24:25] neg_lo:[1,0,0] neg_hi:[1,0,0]
	v_mov_b32_e32 v24, v42
	v_mov_b32_e32 v25, v54
	v_mul_f32_e32 v30, v54, v54
	v_pk_fma_f32 v[74:75], v[24:25], v[24:25], v[30:31] op_sel_hi:[1,1,0]
	v_mov_b32_e32 v24, v43
	v_mov_b32_e32 v25, v55
	v_mul_f32_e32 v30, v55, v55
	v_pk_fma_f32 v[84:85], v[24:25], v[24:25], v[30:31] op_sel_hi:[1,1,0]
	v_lshlrev_b32_e32 v25, 16, v87
	v_lshlrev_b32_e32 v24, 16, v86
	v_lshlrev_b32_e32 v31, 16, v89
	v_lshlrev_b32_e32 v30, 16, v88
	v_pk_fma_f32 v[24:25], v[214:215], v[30:31], v[24:25] neg_lo:[1,0,0] neg_hi:[1,0,0]
	v_and_b32_e32 v31, 0xffff0000, v87
	v_and_b32_e32 v30, 0xffff0000, v86
	v_and_b32_e32 v87, 0xffff0000, v89
	v_and_b32_e32 v86, 0xffff0000, v88
	v_pk_fma_f32 v[30:31], v[214:215], v[86:87], v[30:31] neg_lo:[1,0,0] neg_hi:[1,0,0]
	v_pk_mul_f32 v[86:87], v[24:25], v[24:25]
	v_pk_mul_f32 v[88:89], v[30:31], v[30:31]
	v_mov_b32_e32 v93, v86
	v_mov_b32_e32 v61, v88
	v_mov_b32_e32 v75, v87
	v_mov_b32_e32 v85, v89
	v_pk_add_f32 v[60:61], v[92:93], v[60:61]
	v_pk_add_f32 v[74:75], v[74:75], v[84:85]
	v_lshlrev_b32_e32 v89, 16, v37
	v_pk_add_f32 v[60:61], v[60:61], v[74:75]
	v_lshlrev_b32_e32 v75, 16, v29
	v_pk_add_f32 v[84:85], v[60:61], v[60:61] op_sel:[0,1] op_sel_hi:[1,0]
	v_lshlrev_b32_e32 v61, 16, v91
	v_lshlrev_b32_e32 v60, 16, v90
	v_lshlrev_b32_e32 v74, 16, v28
	v_pk_fma_f32 v[60:61], v[214:215], v[74:75], v[60:61] neg_lo:[1,0,0] neg_hi:[1,0,0]
	v_and_b32_e32 v75, 0xffff0000, v91
	v_and_b32_e32 v74, 0xffff0000, v90
	v_and_b32_e32 v29, 0xffff0000, v29
	v_and_b32_e32 v28, 0xffff0000, v28
	v_pk_fma_f32 v[74:75], v[214:215], v[28:29], v[74:75] neg_lo:[1,0,0] neg_hi:[1,0,0]
	v_lshlrev_b32_e32 v88, 16, v36
	v_pk_mul_f32 v[28:29], v[74:75], v[74:75]
	v_and_b32_e32 v37, 0xffff0000, v37
	v_pk_fma_f32 v[28:29], v[60:61], v[60:61], v[28:29]
	v_and_b32_e32 v36, 0xffff0000, v36
	v_pk_add_f32 v[86:87], v[28:29], v[28:29] op_sel:[0,1] op_sel_hi:[1,0]
	v_lshlrev_b32_e32 v29, 16, v59
	v_lshlrev_b32_e32 v28, 16, v58
	v_and_b32_e32 v59, 0xffff0000, v59
	v_and_b32_e32 v58, 0xffff0000, v58
	v_pk_fma_f32 v[28:29], v[214:215], v[88:89], v[28:29] neg_lo:[1,0,0] neg_hi:[1,0,0]
	v_pk_fma_f32 v[36:37], v[214:215], v[36:37], v[58:59] neg_lo:[1,0,0] neg_hi:[1,0,0]
	v_mov_b32_e32 v58, v28
	v_mov_b32_e32 v59, v36
	v_mul_f32_e32 v88, v36, v36
	v_pk_fma_f32 v[88:89], v[58:59], v[58:59], v[88:89] op_sel_hi:[1,1,0]
	v_mov_b32_e32 v58, v29
	v_mov_b32_e32 v59, v37
	v_mul_f32_e32 v90, v37, v37
	v_pk_fma_f32 v[90:91], v[58:59], v[58:59], v[90:91] op_sel_hi:[1,1,0]
	v_lshlrev_b32_e32 v59, 16, v67
	v_lshlrev_b32_e32 v58, 16, v66
	v_lshlrev_b32_e32 v93, 16, v45
	v_lshlrev_b32_e32 v92, 16, v44
	v_and_b32_e32 v67, 0xffff0000, v67
	v_and_b32_e32 v66, 0xffff0000, v66
	v_and_b32_e32 v45, 0xffff0000, v45
	v_and_b32_e32 v44, 0xffff0000, v44
	v_pk_fma_f32 v[58:59], v[214:215], v[92:93], v[58:59] neg_lo:[1,0,0] neg_hi:[1,0,0]
	v_pk_fma_f32 v[66:67], v[214:215], v[44:45], v[66:67] neg_lo:[1,0,0] neg_hi:[1,0,0]
	v_pk_mul_f32 v[44:45], v[58:59], v[58:59]
	v_pk_mul_f32 v[92:93], v[66:67], v[66:67]
	v_mov_b32_e32 v85, v44
	v_mov_b32_e32 v87, v92
	v_mov_b32_e32 v89, v45
	v_mov_b32_e32 v91, v93
	v_pk_add_f32 v[84:85], v[84:85], v[86:87]
	v_pk_add_f32 v[44:45], v[88:89], v[90:91]
	v_lshlrev_b32_e32 v87, 16, v53
	v_pk_add_f32 v[44:45], v[84:85], v[44:45]
	v_lshlrev_b32_e32 v86, 16, v52
	v_pk_add_f32 v[84:85], v[44:45], v[44:45] op_sel:[0,1] op_sel_hi:[1,0]
	v_lshlrev_b32_e32 v45, 16, v63
	v_lshlrev_b32_e32 v44, 16, v62
	v_and_b32_e32 v63, 0xffff0000, v63
	v_and_b32_e32 v62, 0xffff0000, v62
	v_and_b32_e32 v53, 0xffff0000, v53
	v_and_b32_e32 v52, 0xffff0000, v52
	v_pk_fma_f32 v[52:53], v[214:215], v[52:53], v[62:63] neg_lo:[1,0,0] neg_hi:[1,0,0]
	v_pk_fma_f32 v[44:45], v[214:215], v[86:87], v[44:45] neg_lo:[1,0,0] neg_hi:[1,0,0]
	v_pk_mul_f32 v[62:63], v[52:53], v[52:53]
	v_lshlrev_b32_e32 v89, 16, v33
	v_pk_fma_f32 v[62:63], v[44:45], v[44:45], v[62:63]
	v_lshlrev_b32_e32 v88, 16, v32
	v_pk_add_f32 v[86:87], v[62:63], v[62:63] op_sel:[0,1] op_sel_hi:[1,0]
	v_lshlrev_b32_e32 v63, 16, v77
	v_lshlrev_b32_e32 v62, 16, v76
	v_and_b32_e32 v77, 0xffff0000, v77
	v_and_b32_e32 v76, 0xffff0000, v76
	v_and_b32_e32 v33, 0xffff0000, v33
	v_and_b32_e32 v32, 0xffff0000, v32
	v_pk_fma_f32 v[62:63], v[214:215], v[88:89], v[62:63] neg_lo:[1,0,0] neg_hi:[1,0,0]
	v_pk_fma_f32 v[76:77], v[214:215], v[32:33], v[76:77] neg_lo:[1,0,0] neg_hi:[1,0,0]
	v_mov_b32_e32 v32, v62
	v_mov_b32_e32 v33, v76
	v_mul_f32_e32 v88, v76, v76
	v_pk_fma_f32 v[88:89], v[32:33], v[32:33], v[88:89] op_sel_hi:[1,1,0]
	v_mov_b32_e32 v32, v63
	v_mov_b32_e32 v33, v77
	v_mul_f32_e32 v90, v77, v77
	v_pk_fma_f32 v[90:91], v[32:33], v[32:33], v[90:91] op_sel_hi:[1,1,0]
	v_lshlrev_b32_e32 v33, 16, v69
	v_lshlrev_b32_e32 v32, 16, v68
	v_lshlrev_b32_e32 v93, 16, v39
	v_lshlrev_b32_e32 v92, 16, v38
	v_and_b32_e32 v69, 0xffff0000, v69
	v_and_b32_e32 v68, 0xffff0000, v68
	v_and_b32_e32 v39, 0xffff0000, v39
	v_and_b32_e32 v38, 0xffff0000, v38
	v_pk_fma_f32 v[32:33], v[214:215], v[92:93], v[32:33] neg_lo:[1,0,0] neg_hi:[1,0,0]
	v_pk_fma_f32 v[38:39], v[214:215], v[38:39], v[68:69] neg_lo:[1,0,0] neg_hi:[1,0,0]
	v_pk_mul_f32 v[68:69], v[32:33], v[32:33]
	v_pk_mul_f32 v[92:93], v[38:39], v[38:39]
	v_mov_b32_e32 v85, v68
	v_mov_b32_e32 v87, v92
	v_mov_b32_e32 v89, v69
	v_mov_b32_e32 v91, v93
	v_pk_add_f32 v[84:85], v[84:85], v[86:87]
	v_pk_add_f32 v[68:69], v[88:89], v[90:91]
	v_lshlrev_b32_e32 v87, 16, v21
	v_pk_add_f32 v[68:69], v[84:85], v[68:69]
	v_lshlrev_b32_e32 v86, 16, v20
	v_pk_add_f32 v[84:85], v[68:69], v[68:69] op_sel:[0,1] op_sel_hi:[1,0]
	v_lshlrev_b32_e32 v69, 16, v81
	v_lshlrev_b32_e32 v68, 16, v80
	v_and_b32_e32 v81, 0xffff0000, v81
	v_and_b32_e32 v80, 0xffff0000, v80
	v_and_b32_e32 v21, 0xffff0000, v21
	v_and_b32_e32 v20, 0xffff0000, v20
	v_pk_fma_f32 v[80:81], v[214:215], v[20:21], v[80:81] neg_lo:[1,0,0] neg_hi:[1,0,0]
	v_pk_fma_f32 v[68:69], v[214:215], v[86:87], v[68:69] neg_lo:[1,0,0] neg_hi:[1,0,0]
	v_pk_mul_f32 v[20:21], v[80:81], v[80:81]
	v_lshlrev_b32_e32 v89, 16, v23
	v_pk_fma_f32 v[20:21], v[68:69], v[68:69], v[20:21]
	v_lshlrev_b32_e32 v88, 16, v22
	v_pk_add_f32 v[86:87], v[20:21], v[20:21] op_sel:[0,1] op_sel_hi:[1,0]
	v_lshlrev_b32_e32 v21, 16, v47
	v_lshlrev_b32_e32 v20, 16, v46
	v_and_b32_e32 v47, 0xffff0000, v47
	v_and_b32_e32 v46, 0xffff0000, v46
	v_and_b32_e32 v23, 0xffff0000, v23
	v_and_b32_e32 v22, 0xffff0000, v22
	v_pk_fma_f32 v[20:21], v[214:215], v[88:89], v[20:21] neg_lo:[1,0,0] neg_hi:[1,0,0]
	v_pk_fma_f32 v[22:23], v[214:215], v[22:23], v[46:47] neg_lo:[1,0,0] neg_hi:[1,0,0]
	v_mov_b32_e32 v46, v20
	v_mov_b32_e32 v47, v22
	v_mul_f32_e32 v88, v22, v22
	v_pk_fma_f32 v[88:89], v[46:47], v[46:47], v[88:89] op_sel_hi:[1,1,0]
	v_mov_b32_e32 v46, v21
	v_mov_b32_e32 v47, v23
	v_mul_f32_e32 v90, v23, v23
	v_pk_fma_f32 v[90:91], v[46:47], v[46:47], v[90:91] op_sel_hi:[1,1,0]
	v_lshlrev_b32_e32 v47, 16, v57
	v_lshlrev_b32_e32 v46, 16, v56
	v_lshlrev_b32_e32 v93, 16, v49
	v_lshlrev_b32_e32 v92, 16, v48
	v_and_b32_e32 v57, 0xffff0000, v57
	v_and_b32_e32 v56, 0xffff0000, v56
	v_and_b32_e32 v49, 0xffff0000, v49
	v_and_b32_e32 v48, 0xffff0000, v48
	v_pk_fma_f32 v[46:47], v[214:215], v[92:93], v[46:47] neg_lo:[1,0,0] neg_hi:[1,0,0]
	v_pk_fma_f32 v[48:49], v[214:215], v[48:49], v[56:57] neg_lo:[1,0,0] neg_hi:[1,0,0]
	v_pk_mul_f32 v[56:57], v[46:47], v[46:47]
	v_pk_mul_f32 v[92:93], v[48:49], v[48:49]
	v_mov_b32_e32 v85, v56
	v_mov_b32_e32 v87, v92
	v_mov_b32_e32 v89, v57
	v_mov_b32_e32 v91, v93
	v_pk_add_f32 v[84:85], v[84:85], v[86:87]
	v_pk_add_f32 v[56:57], v[88:89], v[90:91]
	v_mov_b32_e32 v10, v9
	v_pk_add_f32 v[56:57], v[84:85], v[56:57]
	s_nop 0
	v_add_f32_e32 v56, v56, v57
	ds_bpermute_b32 v57, v83, v56
	s_waitcnt lgkmcnt(0)
	v_add_f32_e32 v2, v56, v57
	v_fmamk_f32 v2, v2, 0x3c000000, v1
	v_mul_f32_e32 v14, 0x4f800000, v2
	v_cmp_gt_f32_e32 vcc, s0, v2
	s_nop 1
	v_cndmask_b32_e32 v2, v2, v14, vcc
	v_sqrt_f32_e32 v56, v2
	v_mov_b32_e32 v14, v8
	v_add_u32_e32 v8, -1, v56
	v_fma_f32 v9, -v8, v56, v2
	v_cmp_ge_f32_e64 s[0:1], 0, v9
	v_add_u32_e32 v9, 1, v56
	s_nop 0
	v_cndmask_b32_e64 v8, v56, v8, s[0:1]
	v_fma_f32 v56, -v9, v56, v2
	v_cmp_lt_f32_e64 s[0:1], 0, v56
	s_nop 1
	v_cndmask_b32_e64 v8, v8, v9, s[0:1]
	v_mul_f32_e32 v9, 0x37800000, v8
	v_cndmask_b32_e32 v8, v8, v9, vcc
	v_cmp_class_f32_e32 vcc, v2, v226
	v_mov_b32_e32 v9, v6
	v_mov_b32_e32 v6, v5
	v_cndmask_b32_e32 v2, v8, v2, vcc
	v_div_scale_f32 v56, s[0:1], v2, v2, 1.0
	v_rcp_f32_e32 v57, v56
	v_mov_b32_e32 v8, v4
	v_fma_f32 v4, -v56, v57, 1.0
	v_fmac_f32_e32 v57, v4, v57
	v_div_scale_f32 v4, vcc, 1.0, v2, 1.0
	v_mul_f32_e32 v5, v4, v57
	v_fma_f32 v83, -v56, v5, v4
	v_fmac_f32_e32 v5, v83, v57
	v_fma_f32 v4, -v56, v5, v4
	v_div_fmas_f32 v4, v4, v57, v5
	v_div_fixup_f32 v2, v4, v2, 1.0
	v_mul_f32_e32 v2, 0x3f4ccccd, v2
	v_pk_mul_f32 v[4:5], v[78:79], v[2:3] op_sel_hi:[1,0]
	v_pk_mul_f32 v[16:17], v[16:17], v[2:3] op_sel_hi:[1,0]
	v_pk_mul_f32 v[4:5], v[14:15], v[4:5]
	v_pk_mul_f32 v[14:15], v[72:73], v[2:3] op_sel_hi:[1,0]
	s_nop 0
	v_pk_mul_f32 v[10:11], v[10:11], v[14:15]
	v_pk_mul_f32 v[14:15], v[70:71], v[2:3] op_sel_hi:[1,0]
	v_pk_mul_f32 v[8:9], v[8:9], v[14:15]
	v_pk_mul_f32 v[14:15], v[64:65], v[2:3] op_sel_hi:[1,0]
	v_pk_mul_f32 v[6:7], v[6:7], v[14:15]
	v_cvt_pk_bf16_f32 v7, v9, v7
	v_cvt_pk_bf16_f32 v6, v8, v6
	v_cvt_pk_bf16_f32 v5, v5, v11
	v_cvt_pk_bf16_f32 v4, v4, v10
	global_store_dwordx4 v[12:13], v[4:7], off offset:1024
	global_load_dwordx4 v[4:7], v82, s[58:59] offset:32
	s_nop 0
	global_load_dwordx4 v[8:11], v82, s[58:59] offset:48
	v_pk_mul_f32 v[14:15], v[18:19], v[2:3] op_sel_hi:[1,0]
	s_waitcnt vmcnt(1)
	v_mov_b32_e32 v19, v6
	v_mov_b32_e32 v6, v5
	v_mov_b32_e32 v18, v4
	v_pk_mul_f32 v[4:5], v[6:7], v[16:17]
	v_pk_mul_f32 v[6:7], v[40:41], v[2:3] op_sel_hi:[1,0]
	s_waitcnt vmcnt(0)
	v_mov_b32_e32 v16, v8
	v_mov_b32_e32 v17, v10
	v_pk_mul_f32 v[6:7], v[16:17], v[6:7]
	v_pk_mul_f32 v[16:17], v[50:51], v[2:3] op_sel_hi:[1,0]
	v_mov_b32_e32 v10, v9
	v_pk_mul_f32 v[8:9], v[10:11], v[16:17]
	v_pk_mul_f32 v[14:15], v[18:19], v[14:15]
	v_bfe_u32 v10, v9, 16, 1
	v_bfe_u32 v11, v8, 16, 1
	v_add3_u32 v8, v8, v11, s81
	v_add3_u32 v9, v9, v10, s81
	v_bfe_u32 v16, v6, 16, 1
	v_bfe_u32 v17, v7, 16, 1
	v_add3_u32 v7, v7, v17, s81
	v_add3_u32 v6, v6, v16, s81
	v_lshrrev_b32_e32 v6, 16, v6
	v_lshrrev_b32_e32 v7, 16, v7
	v_and_or_b32 v7, v9, s80, v7
	v_and_or_b32 v6, v8, s80, v6
	v_cvt_pk_bf16_f32 v5, v15, v5
	v_cvt_pk_bf16_f32 v4, v14, v4
	global_store_dwordx4 v[12:13], v[4:7], off offset:1040
	global_load_dwordx4 v[4:7], v82, s[58:59] offset:64
	s_nop 0
	global_load_dwordx4 v[8:11], v82, s[58:59] offset:80
	v_pk_mul_f32 v[14:15], v[26:27], v[2:3] op_sel_hi:[1,0]
	v_pk_mul_f32 v[18:19], v[62:63], v[2:3] op_sel_hi:[1,0]
	s_waitcnt vmcnt(1)
	v_mov_b32_e32 v16, v4
	v_mov_b32_e32 v17, v6
	v_pk_mul_f32 v[14:15], v[14:15], v[16:17]
	v_pk_mul_f32 v[16:17], v[34:35], v[2:3] op_sel_hi:[1,0]
	v_mov_b32_e32 v6, v5
	v_pk_mul_f32 v[4:5], v[16:17], v[6:7]
	v_pk_mul_f32 v[6:7], v[42:43], v[2:3] op_sel_hi:[1,0]
	s_waitcnt vmcnt(0)
	v_mov_b32_e32 v16, v8
	v_mov_b32_e32 v17, v10
	v_pk_mul_f32 v[6:7], v[6:7], v[16:17]
	v_pk_mul_f32 v[16:17], v[54:55], v[2:3] op_sel_hi:[1,0]
	v_mov_b32_e32 v10, v9
	v_pk_mul_f32 v[8:9], v[16:17], v[10:11]
	v_bfe_u32 v10, v9, 16, 1
	v_bfe_u32 v11, v8, 16, 1
	v_add3_u32 v8, v8, v11, s81
	v_add3_u32 v9, v9, v10, s81
	v_bfe_u32 v16, v6, 16, 1
	v_bfe_u32 v17, v7, 16, 1
	v_add3_u32 v7, v7, v17, s81
	v_add3_u32 v6, v6, v16, s81
	v_lshrrev_b32_e32 v6, 16, v6
	v_lshrrev_b32_e32 v7, 16, v7
	v_and_or_b32 v7, v9, s80, v7
	v_and_or_b32 v6, v8, s80, v6
	v_cvt_pk_bf16_f32 v5, v15, v5
	v_cvt_pk_bf16_f32 v4, v14, v4
	global_store_dwordx4 v[12:13], v[4:7], off offset:1056
	global_load_dwordx4 v[4:7], v82, s[58:59] offset:96
	s_nop 0
	global_load_dwordx4 v[8:11], v82, s[58:59] offset:112
	v_pk_mul_f32 v[14:15], v[24:25], v[2:3] op_sel_hi:[1,0]
	v_pk_mul_f32 v[24:25], v[76:77], v[2:3] op_sel_hi:[1,0]
	s_waitcnt vmcnt(1)
	v_mov_b32_e32 v16, v4
	v_mov_b32_e32 v17, v6
	v_pk_mul_f32 v[14:15], v[14:15], v[16:17]
	v_pk_mul_f32 v[16:17], v[30:31], v[2:3] op_sel_hi:[1,0]
	v_mov_b32_e32 v6, v5
	v_pk_mul_f32 v[4:5], v[16:17], v[6:7]
	v_pk_mul_f32 v[6:7], v[60:61], v[2:3] op_sel_hi:[1,0]
	s_waitcnt vmcnt(0)
	v_mov_b32_e32 v16, v8
	v_mov_b32_e32 v17, v10
	v_pk_mul_f32 v[6:7], v[6:7], v[16:17]
	v_pk_mul_f32 v[16:17], v[74:75], v[2:3] op_sel_hi:[1,0]
	v_mov_b32_e32 v10, v9
	v_pk_mul_f32 v[8:9], v[16:17], v[10:11]
	v_bfe_u32 v10, v9, 16, 1
	v_bfe_u32 v11, v8, 16, 1
	v_add3_u32 v8, v8, v11, s81
	v_add3_u32 v9, v9, v10, s81
	v_bfe_u32 v16, v6, 16, 1
	v_bfe_u32 v17, v7, 16, 1
	v_add3_u32 v7, v7, v17, s81
	v_add3_u32 v6, v6, v16, s81
	v_lshrrev_b32_e32 v6, 16, v6
	v_lshrrev_b32_e32 v7, 16, v7
	v_and_or_b32 v7, v9, s80, v7
	v_and_or_b32 v6, v8, s80, v6
	v_cvt_pk_bf16_f32 v5, v15, v5
	v_cvt_pk_bf16_f32 v4, v14, v4
	global_store_dwordx4 v[12:13], v[4:7], off offset:1072
	global_load_dwordx4 v[4:7], v82, s[58:59] offset:128
	s_nop 0
	global_load_dwordx4 v[8:11], v82, s[58:59] offset:144
	v_pk_mul_f32 v[14:15], v[28:29], v[2:3] op_sel_hi:[1,0]
	s_waitcnt vmcnt(1)
	v_mov_b32_e32 v16, v4
	v_mov_b32_e32 v17, v6
	v_pk_mul_f32 v[14:15], v[14:15], v[16:17]
	v_pk_mul_f32 v[16:17], v[36:37], v[2:3] op_sel_hi:[1,0]
	v_mov_b32_e32 v6, v5
	v_pk_mul_f32 v[4:5], v[16:17], v[6:7]
	v_pk_mul_f32 v[6:7], v[58:59], v[2:3] op_sel_hi:[1,0]
	s_waitcnt vmcnt(0)
	v_mov_b32_e32 v16, v8
	v_mov_b32_e32 v17, v10
	v_pk_mul_f32 v[6:7], v[6:7], v[16:17]
	v_pk_mul_f32 v[16:17], v[66:67], v[2:3] op_sel_hi:[1,0]
	v_mov_b32_e32 v10, v9
	v_pk_mul_f32 v[8:9], v[16:17], v[10:11]
	v_bfe_u32 v10, v9, 16, 1
	v_bfe_u32 v11, v8, 16, 1
	v_add3_u32 v8, v8, v11, s81
	v_add3_u32 v9, v9, v10, s81
	v_bfe_u32 v16, v6, 16, 1
	v_bfe_u32 v17, v7, 16, 1
	v_add3_u32 v7, v7, v17, s81
	v_add3_u32 v6, v6, v16, s81
	v_lshrrev_b32_e32 v6, 16, v6
	v_lshrrev_b32_e32 v7, 16, v7
	v_and_or_b32 v7, v9, s80, v7
	v_and_or_b32 v6, v8, s80, v6
	v_cvt_pk_bf16_f32 v5, v15, v5
	v_cvt_pk_bf16_f32 v4, v14, v4
	global_store_dwordx4 v[12:13], v[4:7], off offset:1088
	global_load_dwordx4 v[4:7], v82, s[58:59] offset:160
	s_nop 0
	global_load_dwordx4 v[8:11], v82, s[58:59] offset:176
	v_pk_mul_f32 v[16:17], v[52:53], v[2:3] op_sel_hi:[1,0]
	v_pk_mul_f32 v[14:15], v[44:45], v[2:3] op_sel_hi:[1,0]
	s_waitcnt vmcnt(1)
	v_mov_b32_e32 v27, v6
	v_mov_b32_e32 v6, v5
	s_waitcnt vmcnt(0)
	v_mov_b32_e32 v5, v10
	v_mov_b32_e32 v10, v9
	v_mov_b32_e32 v26, v4
	v_mov_b32_e32 v4, v8
	v_pk_mul_f32 v[6:7], v[16:17], v[6:7]
	v_pk_mul_f32 v[10:11], v[24:25], v[10:11]
	v_pk_mul_f32 v[8:9], v[14:15], v[26:27]
	v_pk_mul_f32 v[4:5], v[18:19], v[4:5]
	v_bfe_u32 v14, v11, 16, 1
	v_bfe_u32 v15, v10, 16, 1
	v_bfe_u32 v16, v7, 16, 1
	v_bfe_u32 v17, v6, 16, 1
	v_add3_u32 v17, v6, v17, s81
	v_add3_u32 v16, v7, v16, s81
	v_add3_u32 v6, v10, v15, s81
	v_add3_u32 v7, v11, v14, s81
	v_bfe_u32 v10, v8, 16, 1
	v_bfe_u32 v11, v9, 16, 1
	v_bfe_u32 v14, v4, 16, 1
	v_bfe_u32 v15, v5, 16, 1
	v_add3_u32 v5, v5, v15, s81
	v_add3_u32 v4, v4, v14, s81
	v_add3_u32 v9, v9, v11, s81
	v_add3_u32 v8, v8, v10, s81
	v_lshrrev_b32_e32 v8, 16, v8
	v_lshrrev_b32_e32 v9, 16, v9
	v_lshrrev_b32_e32 v4, 16, v4
	v_lshrrev_b32_e32 v5, 16, v5
	v_and_or_b32 v7, v7, s80, v5
	v_and_or_b32 v6, v6, s80, v4
	v_and_or_b32 v5, v16, s80, v9
	v_and_or_b32 v4, v17, s80, v8
	global_store_dwordx4 v[12:13], v[4:7], off offset:1104
	global_load_dwordx4 v[4:7], v82, s[58:59] offset:192
	s_nop 0
	global_load_dwordx4 v[8:11], v82, s[58:59] offset:208
	v_pk_mul_f32 v[14:15], v[32:33], v[2:3] op_sel_hi:[1,0]
	v_pk_mul_f32 v[18:19], v[68:69], v[2:3] op_sel_hi:[1,0]
	v_pk_mul_f32 v[16:17], v[38:39], v[2:3] op_sel_hi:[1,0]
	v_pk_mul_f32 v[24:25], v[80:81], v[2:3] op_sel_hi:[1,0]
	s_waitcnt vmcnt(1)
	v_mov_b32_e32 v26, v4
	v_mov_b32_e32 v27, v6
	v_mov_b32_e32 v6, v5
	s_waitcnt vmcnt(0)
	v_mov_b32_e32 v4, v8
	v_mov_b32_e32 v5, v10
	v_mov_b32_e32 v10, v9
	v_pk_mul_f32 v[8:9], v[14:15], v[26:27]
	v_pk_mul_f32 v[4:5], v[18:19], v[4:5]
	v_pk_mul_f32 v[6:7], v[16:17], v[6:7]
	v_pk_mul_f32 v[10:11], v[24:25], v[10:11]
	v_bfe_u32 v18, v8, 16, 1
	v_bfe_u32 v19, v9, 16, 1
	v_bfe_u32 v16, v7, 16, 1
	v_bfe_u32 v17, v6, 16, 1
	v_add3_u32 v9, v9, v19, s81
	v_add3_u32 v8, v8, v18, s81
	v_add3_u32 v17, v6, v17, s81
	v_add3_u32 v16, v7, v16, s81
	v_lshrrev_b32_e32 v8, 16, v8
	v_lshrrev_b32_e32 v9, 16, v9
	v_cvt_pk_bf16_f32 v7, v5, v11
	v_cvt_pk_bf16_f32 v6, v4, v10
	v_and_or_b32 v5, v16, s80, v9
	v_and_or_b32 v4, v17, s80, v8
	global_store_dwordx4 v[12:13], v[4:7], off offset:1120
	global_load_dwordx4 v[4:7], v82, s[58:59] offset:224
	s_nop 0
	global_load_dwordx4 v[8:11], v82, s[58:59] offset:240
	v_pk_mul_f32 v[14:15], v[20:21], v[2:3] op_sel_hi:[1,0]
	v_pk_mul_f32 v[16:17], v[22:23], v[2:3] op_sel_hi:[1,0]
	v_pk_mul_f32 v[18:19], v[46:47], v[2:3] op_sel_hi:[1,0]
	v_pk_mul_f32 v[20:21], v[48:49], v[2:3] op_sel_hi:[1,0]
	s_waitcnt vmcnt(1)
	v_mov_b32_e32 v22, v4
	v_mov_b32_e32 v23, v6
	v_mov_b32_e32 v6, v5
	s_waitcnt vmcnt(0)
	v_mov_b32_e32 v4, v8
	v_mov_b32_e32 v5, v10
	v_mov_b32_e32 v10, v9
	v_pk_mul_f32 v[8:9], v[14:15], v[22:23]
	v_pk_mul_f32 v[6:7], v[16:17], v[6:7]
	v_pk_mul_f32 v[4:5], v[18:19], v[4:5]
	v_pk_mul_f32 v[10:11], v[20:21], v[10:11]
	v_bfe_u32 v15, v7, 16, 1
	v_bfe_u32 v17, v8, 16, 1
	v_bfe_u32 v18, v9, 16, 1
	v_bfe_u32 v19, v4, 16, 1
	v_bfe_u32 v14, v10, 16, 1
	v_bfe_u32 v16, v6, 16, 1
	v_add3_u32 v15, v7, v15, s81
	v_add3_u32 v4, v4, v19, s81
	v_add3_u32 v7, v9, v18, s81
	v_add3_u32 v8, v8, v17, s81
	v_add3_u32 v16, v6, v16, s81
	v_add3_u32 v6, v10, v14, s81
	v_lshrrev_b32_e32 v8, 16, v8
	v_lshrrev_b32_e32 v9, 16, v7
	v_lshrrev_b32_e32 v4, 16, v4
	v_cvt_pk_bf16_f32 v7, v5, v11
	v_and_or_b32 v6, v6, s80, v4
	v_and_or_b32 v5, v15, s80, v9
	v_and_or_b32 v4, v16, s80, v8
	global_store_dwordx4 v[12:13], v[4:7], off offset:1136
	s_branch .LBB0_259
.LBB0_346:
	v_max_f32_e32 v16, v16, v16
	v_max_f32_e32 v17, 0, v16
	v_exp_f32_e64 v16, -v17
	v_cmp_gt_u32_e32 vcc, 32, v230
	s_and_saveexec_b64 s[2:3], vcc
	ds_write_b32 v235, v16
	s_or_b64 exec, exec, s[2:3]
	v_sub_f32_e32 v113, v113, v17
	v_sub_f32_e32 v112, v112, v17
	v_sub_f32_e32 v111, v111, v17
	v_sub_f32_e32 v110, v110, v17
	v_sub_f32_e32 v109, v109, v17
	v_sub_f32_e32 v108, v108, v17
	v_sub_f32_e32 v107, v107, v17
	v_sub_f32_e32 v106, v106, v17
	v_sub_f32_e32 v105, v105, v17
	v_sub_f32_e32 v104, v104, v17
	v_sub_f32_e32 v103, v103, v17
	v_sub_f32_e32 v102, v102, v17
	v_sub_f32_e32 v101, v101, v17
	v_sub_f32_e32 v100, v100, v17
	v_sub_f32_e32 v99, v99, v17
	v_sub_f32_e32 v98, v98, v17
	v_sub_f32_e32 v97, v97, v17
	v_sub_f32_e32 v96, v96, v17
	v_sub_f32_e32 v95, v95, v17
	v_sub_f32_e32 v94, v94, v17
	v_sub_f32_e32 v93, v93, v17
	v_sub_f32_e32 v92, v92, v17
	v_sub_f32_e32 v91, v91, v17
	v_sub_f32_e32 v90, v90, v17
	v_sub_f32_e32 v89, v89, v17
	v_sub_f32_e32 v88, v88, v17
	v_sub_f32_e32 v87, v87, v17
	v_sub_f32_e32 v86, v86, v17
	v_sub_f32_e32 v85, v85, v17
	v_sub_f32_e32 v84, v84, v17
	v_sub_f32_e32 v83, v83, v17
	v_sub_f32_e32 v82, v82, v17
	v_mul_f32_e32 v243, v243, v16
	s_branch .LBB0_340
	s_nop 0
	s_nop 0
.LBB0_349:
	v_mov_b32_e32 v52, v0
	s_barrier
	s_ashr_i32 s21, s20, 31
	v_readfirstlane_b32 s0, v52
	s_ashr_i32 s2, s0, 2
	s_and_b32 s36, s2, -16
	s_ashr_i32 s3, s0, 7
	v_lshlrev_b32_e32 v2, 4, v52
	v_and_b32_e32 v38, 48, v52
	v_mov_b32_e32 v39, 0
	v_and_b32_e32 v59, 48, v2
	v_lshl_add_u64 v[2:3], s[22:23], 0, v[38:39]
	s_mov_b64 s[0:1], 0x100000
	s_cmp_gt_i32 s3, -1
	v_lshl_add_u64 v[42:43], v[2:3], 0, s[0:1]
	s_cselect_b64 s[0:1], -1, 0
	s_cmp_gt_i32 s3, 0
	v_ashrrev_i32_e32 v58, 2, v52
	s_cselect_b64 s[24:25], -1, 0
	s_cmp_gt_i32 s3, 1
	s_movk_i32 s4, 0x1200
	v_and_b32_e32 v1, 63, v52
	s_cselect_b64 s[26:27], -1, 0
	s_cmp_gt_i32 s3, 2
	v_bfi_b32 v44, -16, s2, v52
	v_mad_i64_i32 v[2:3], s[2:3], v58, s4, 0
	v_mov_b32_e32 v8, 0x90000
	v_lshlrev_b32_e32 v1, 2, v1
	v_mad_i64_i32 v[2:3], s[2:3], s20, v8, v[2:3]
	v_xor_b32_e32 v45, 4, v1
	v_xor_b32_e32 v53, 8, v1
	s_cselect_b64 s[28:29], -1, 0
	v_and_b32_e32 v1, 3, v52
	s_add_u32 s2, s94, s41
	v_lshl_or_b32 v2, v1, 5, v2
	s_addc_u32 s3, s95, 0
	v_bfe_u32 v41, v52, 4, 2
	v_lshl_add_u64 v[46:47], s[2:3], 0, v[2:3]
	v_mad_i64_i32 v[2:3], s[4:5], v44, s4, 0
	v_lshlrev_b32_e32 v40, 3, v41
	v_mad_i64_i32 v[2:3], s[4:5], s20, v8, v[2:3]
	v_or_b32_e32 v2, v2, v40
	v_and_b32_e32 v55, 15, v52
	v_lshl_add_u64 v[2:3], s[2:3], 0, v[2:3]
	s_mov_b64 s[2:3], 0x10a00040
	v_lshl_add_u32 v4, v58, 1, 0
	v_add_u32_e32 v5, 0, v38
	v_mul_u32_u24_e32 v6, 0x110, v59
	v_mul_u32_u24_e32 v7, 0x110, v55
	v_lshl_add_u64 v[48:49], v[2:3], 0, s[2:3]
	v_cndmask_b32_e64 v2, 0, 1, s[0:1]
	s_mov_b64 s[30:31], 0
	s_mov_b64 s[34:35], 0x10a00200
	v_mov_b32_e32 v39, 0x3727c5ac
	s_mov_b32 s33, 0xf800000
	v_mov_b32_e32 v54, 0x260
	s_movk_i32 s37, 0x7fff
	v_add_u32_e32 v56, v4, v6
	v_cmp_ne_u32_e64 s[2:3], 1, v2
	v_add_u32_e32 v57, v5, v7
	v_mov_b32_e32 v60, 1
	v_readlane_b32 s41, v254, 39
	s_branch .LBB0_351

.LBB0_872:
	s_add_i32 s21, s21, 1
	s_cmp_eq_u32 s21, 4
	s_cbranch_scc1 .LBB0_962
	s_nop 0
	s_nop 0
	s_nop 0
	s_nop 0
	s_nop 0
	s_nop 0
	s_nop 0
	s_nop 0
	s_nop 0
	s_nop 0
	s_nop 0
	s_nop 0
	s_nop 0
	s_nop 0
	s_nop 0
